# speedup vs baseline: 1.0048x; 1.0048x over previous
.LBB0_26:
	s_or_b64 exec, exec, s[26:27]
	s_movk_i32 s8, 0x61a7
	s_waitcnt vmcnt(2)
	v_cmp_lt_u32_e64 s[0:1], s8, v30
	s_mov_b32 s9, 0xc34f
	s_mov_b32 s10, 0x124f7
	v_cndmask_b32_e64 v0, 0, 1, s[0:1]
	v_cmp_lt_u32_e64 s[0:1], s9, v30
	s_movk_i32 s11, 0x1f70
	s_mov_b32 s12, 0x29f17
	s_waitcnt lgkmcnt(0)
	v_cndmask_b32_e64 v1, 0, 1, s[0:1]
	v_cmp_lt_u32_e64 s[0:1], s10, v30
	s_barrier
	s_nop 0
	v_addc_co_u32_e64 v0, s[0:1], v0, v1, s[0:1]
	v_mad_u32_u24 v1, v87, s11, v26
	v_lshlrev_b32_e32 v1, 19, v1
	v_lshl_add_u32 v0, v0, 17, v1
	v_lshlrev_b32_e32 v1, 2, v86
	v_or_b32_e32 v0, v0, v30
	ds_read_b32 v26, v84 offset:52784
	ds_read_b32 v30, v85 offset:52784
	ds_read_b32 v34, v83 offset:52784
	ds_read_b32 v35, v82 offset:52784
	ds_read_b32 v36, v81 offset:52784
	ds_read_b32 v37, v80 offset:52784
	ds_read_b32 v38, v79 offset:52784
	ds_read_b32 v39, v78 offset:52784
	s_waitcnt lgkmcnt(7)
	v_lshl_add_u32 v1, v26, 2, v1
	ds_write_b32 v1, v0
	v_mul_hi_u32_u24_e32 v0, s12, v31
	v_mad_u32_u24 v1, v77, s11, v27
	v_lshlrev_b32_e32 v1, 19, v1
	v_lshl_add_u32 v0, v0, 17, v1
	v_lshlrev_b32_e32 v1, 2, v76
	v_or_b32_e32 v0, v0, v31
	s_waitcnt lgkmcnt(7)
	v_lshl_add_u32 v1, v30, 2, v1
	ds_write_b32 v1, v0
	v_mul_hi_u32_u24_e32 v0, s12, v32
	v_mad_u32_u24 v1, v75, s11, v28
	v_lshlrev_b32_e32 v1, 19, v1
	v_lshl_add_u32 v0, v0, 17, v1
	v_lshlrev_b32_e32 v1, 2, v74
	v_or_b32_e32 v0, v0, v32
	s_waitcnt lgkmcnt(7)
	v_lshl_add_u32 v1, v34, 2, v1
	ds_write_b32 v1, v0
	v_mul_hi_u32_u24_e32 v0, s12, v33
	v_mad_u32_u24 v1, v73, s11, v29
	v_lshlrev_b32_e32 v1, 19, v1
	v_lshl_add_u32 v0, v0, 17, v1
	v_lshlrev_b32_e32 v1, 2, v72
	v_or_b32_e32 v0, v0, v33
	s_waitcnt lgkmcnt(7)
	v_lshl_add_u32 v1, v35, 2, v1
	s_waitcnt vmcnt(1)
	ds_write_b32 v1, v0
	v_mul_hi_u32_u24_e32 v0, s12, v22
	v_mad_u32_u24 v1, v71, s11, v18
	v_lshlrev_b32_e32 v1, 19, v1
	v_lshl_add_u32 v0, v0, 17, v1
	v_lshlrev_b32_e32 v1, 2, v70
	v_or_b32_e32 v0, v0, v22
	s_waitcnt lgkmcnt(7)
	v_lshl_add_u32 v1, v36, 2, v1
	ds_write_b32 v1, v0
	v_mul_hi_u32_u24_e32 v0, s12, v23
	v_mad_u32_u24 v1, v69, s11, v19
	v_lshlrev_b32_e32 v1, 19, v1
	v_lshl_add_u32 v0, v0, 17, v1
	v_lshlrev_b32_e32 v1, 2, v68
	v_or_b32_e32 v0, v0, v23
	s_waitcnt lgkmcnt(7)
	v_lshl_add_u32 v1, v37, 2, v1
	ds_write_b32 v1, v0
	v_mul_hi_u32_u24_e32 v0, s12, v24
	v_mad_u32_u24 v1, v67, s11, v20
	v_lshlrev_b32_e32 v1, 19, v1
	v_lshl_add_u32 v0, v0, 17, v1
	v_lshlrev_b32_e32 v1, 2, v66
	v_or_b32_e32 v0, v0, v24
	s_waitcnt lgkmcnt(7)
	v_lshl_add_u32 v1, v38, 2, v1
	ds_write_b32 v1, v0
	v_mul_hi_u32_u24_e32 v0, s12, v25
	v_mad_u32_u24 v1, v65, s11, v21
	v_lshlrev_b32_e32 v1, 19, v1
	v_lshl_add_u32 v0, v0, 17, v1
	v_lshlrev_b32_e32 v1, 2, v63
	v_or_b32_e32 v0, v0, v25
	s_waitcnt lgkmcnt(7)
	v_lshl_add_u32 v1, v39, 2, v1
	s_waitcnt vmcnt(0)
	ds_write_b32 v1, v0
	ds_read_b32 v0, v64 offset:52784
	v_mul_hi_u32_u24_e32 v1, s12, v14
	v_mad_u32_u24 v10, v62, s11, v10
	v_lshlrev_b32_e32 v10, 19, v10
	v_lshl_add_u32 v1, v1, 17, v10
	v_lshlrev_b32_e32 v10, 2, v60
	v_or_b32_e32 v1, v1, v14
	s_waitcnt lgkmcnt(0)
	v_lshl_add_u32 v0, v0, 2, v10
	ds_read_b32 v14, v61 offset:52784
	ds_read_b32 v18, v59 offset:52784
	ds_read_b32 v19, v58 offset:52784
	ds_write_b32 v0, v1
	v_mul_hi_u32_u24_e32 v0, s12, v15
	v_mad_u32_u24 v1, v57, s11, v11
	v_lshlrev_b32_e32 v1, 19, v1
	v_lshl_add_u32 v0, v0, 17, v1
	v_lshlrev_b32_e32 v1, 2, v56
	v_or_b32_e32 v0, v0, v15
	s_waitcnt lgkmcnt(3)
	v_lshl_add_u32 v1, v14, 2, v1
	ds_write_b32 v1, v0
	v_mul_hi_u32_u24_e32 v0, s12, v16
	v_mad_u32_u24 v1, v55, s11, v12
	v_lshlrev_b32_e32 v1, 19, v1
	v_lshl_add_u32 v0, v0, 17, v1
	v_lshlrev_b32_e32 v1, 2, v54
	v_or_b32_e32 v0, v0, v16
	s_waitcnt lgkmcnt(3)
	v_lshl_add_u32 v1, v18, 2, v1
	ds_write_b32 v1, v0
	v_mul_hi_u32_u24_e32 v0, s12, v17
	v_mad_u32_u24 v1, v53, s11, v13
	v_lshlrev_b32_e32 v1, 19, v1
	v_lshl_add_u32 v0, v0, 17, v1
	v_lshlrev_b32_e32 v1, 2, v52
	v_or_b32_e32 v0, v0, v17
	s_waitcnt lgkmcnt(3)
	v_lshl_add_u32 v1, v19, 2, v1
	ds_write_b32 v1, v0
	s_and_saveexec_b64 s[2:3], s[4:5]
	s_cbranch_execz .LBB0_28
	s_mov_b32 s4, 0x38e38e39
	v_mul_hi_u32 v0, v2, s4
	v_lshrrev_b32_e32 v0, 5, v0
	v_cmp_lt_u32_e64 s[0:1], s8, v6
	v_lshlrev_b32_e32 v1, 2, v0
	ds_read_b32 v1, v1 offset:52784
	v_cndmask_b32_e64 v10, 0, 1, s[0:1]
	v_cmp_lt_u32_e64 s[0:1], s9, v6
	v_mad_u32_u24 v0, v0, s11, v2
	v_lshlrev_b32_e32 v0, 19, v0
	v_cndmask_b32_e64 v11, 0, 1, s[0:1]
	v_cmp_lt_u32_e64 s[0:1], s10, v6
	v_mul_hi_u32 v13, v5, s4
	v_lshlrev_b32_e32 v2, 2, v51
	v_addc_co_u32_e64 v10, s[0:1], v10, v11, s[0:1]
	v_lshl_add_u32 v0, v10, 17, v0
	v_or_b32_e32 v0, v0, v6
	v_mul_hi_u32 v6, v3, s4
	v_mul_hi_u32 v11, v4, s4
	v_lshrrev_b32_e32 v6, 5, v6
	v_lshrrev_b32_e32 v11, 5, v11
	v_lshrrev_b32_e32 v13, 5, v13
	v_lshlrev_b32_e32 v10, 2, v6
	v_lshlrev_b32_e32 v12, 2, v11
	v_lshlrev_b32_e32 v14, 2, v13
	s_waitcnt lgkmcnt(0)
	v_lshl_add_u32 v1, v1, 2, v2
	ds_read_b32 v10, v10 offset:52784
	ds_read_b32 v12, v12 offset:52784
	ds_read_b32 v14, v14 offset:52784
	ds_write_b32 v1, v0
	v_mul_hi_u32_u24_e32 v0, s12, v7
	v_mad_u32_u24 v1, v6, s11, v3
	v_lshlrev_b32_e32 v1, 19, v1
	v_lshl_add_u32 v0, v0, 17, v1
	v_lshlrev_b32_e32 v1, 2, v50
	v_or_b32_e32 v0, v0, v7
	s_waitcnt lgkmcnt(3)
	v_lshl_add_u32 v1, v10, 2, v1
	ds_write_b32 v1, v0
	v_mul_hi_u32_u24_e32 v0, s12, v8
	v_mad_u32_u24 v1, v11, s11, v4
	v_lshlrev_b32_e32 v1, 19, v1
	v_lshl_add_u32 v0, v0, 17, v1
	v_lshlrev_b32_e32 v1, 2, v49
	v_or_b32_e32 v0, v0, v8
	s_waitcnt lgkmcnt(3)
	v_lshl_add_u32 v1, v12, 2, v1
	ds_write_b32 v1, v0
	v_mul_hi_u32_u24_e32 v0, s12, v9
	v_mad_u32_u24 v1, v13, s11, v5
	v_lshlrev_b32_e32 v1, 19, v1
	v_lshl_add_u32 v0, v0, 17, v1
	v_lshlrev_b32_e32 v1, 2, v48
	v_or_b32_e32 v0, v0, v9
	s_waitcnt lgkmcnt(3)
	v_lshl_add_u32 v1, v14, 2, v1
	ds_write_b32 v1, v0
